# speedup vs baseline: 1.0106x; 1.0033x over previous
_Z6k_prepPKfS0_PfS1_PdS2_PtS3_S3_:
	s_cmp_gt_u32 s2, 15
	s_cbranch_scc1 .Lmy_pf_skip
	s_getpc_b64 s[28:29]
	v_lshlrev_b32_e32 v29, 6, v0
	v_add_u32_e32 v30, 0x4000, v29
	v_add_u32_e32 v31, 0x8000, v29
	v_min_u32_e32 v31, 0x9d00, v31
	global_load_dword v29, v29, s[28:29]
	global_load_dword v30, v30, s[28:29]
	global_load_dword v31, v31, s[28:29]
.Lmy_pf_skip:
	s_lshl_b32 s12, s2, 4
	s_and_b32 s12, s12, 48
	s_bfe_u32 s13, s2, 0x40003
	s_lshr_b32 s3, s2, 2
	s_or_b32 s19, s12, s13
	s_and_b32 s3, s3, 32
	s_lshl_b32 s12, s19, 6
	s_load_dwordx8 s[4:11], s[0:1], 0x0
	s_bfe_u32 s20, s2, 0x10002
	s_or_b32 s18, s12, s3
	s_and_b32 s14, s2, 0x100
	s_bitcmp1_b32 s2, 8
	s_cselect_b64 s[12:13], -1, 0
	s_cmp_eq_u32 s14, 0
	s_cselect_b64 s[14:15], -1, 0
	s_and_b64 s[16:17], s[14:15], exec
	s_waitcnt lgkmcnt(0)
	s_cselect_b32 s5, s5, s7
	s_cselect_b32 s4, s4, s6
	s_lshl_b32 s6, s20, 21
	s_add_u32 s4, s4, s6
	s_addc_u32 s5, s5, 0
	s_lshl_b32 s6, s18, 2
	s_add_u32 s4, s4, s6
	v_and_b32_e32 v20, 31, v0
	s_addc_u32 s5, s5, 0
	v_lshrrev_b32_e32 v1, 5, v0
	v_lshlrev_b32_e32 v10, 2, v20
	v_mov_b32_e32 v11, 0
	v_lshl_add_u64 v[2:3], s[4:5], 0, v[10:11]
	v_lshlrev_b32_e32 v4, 18, v1
	v_mov_b32_e32 v5, v11
	v_lshl_add_u64 v[2:3], v[2:3], 0, v[4:5]
	s_movk_i32 s4, 0x4000
	v_add_co_u32_e32 v4, vcc, s4, v2
	s_mov_b32 s4, 0x8000
	s_nop 0
	v_addc_co_u32_e32 v5, vcc, 0, v3, vcc
	v_add_co_u32_e32 v6, vcc, s4, v2
	s_mov_b32 s4, 0xc000
	s_nop 0
	v_addc_co_u32_e32 v7, vcc, 0, v3, vcc
	v_add_co_u32_e32 v8, vcc, s4, v2
	s_mov_b32 s4, 0x10000
	s_nop 0
	v_addc_co_u32_e32 v9, vcc, 0, v3, vcc
	v_add_co_u32_e32 v12, vcc, s4, v2
	s_mov_b32 s4, 0x14000
	s_nop 0
	v_addc_co_u32_e32 v13, vcc, 0, v3, vcc
	v_add_co_u32_e32 v14, vcc, s4, v2
	s_mov_b32 s4, 0x18000
	s_nop 0
	v_addc_co_u32_e32 v15, vcc, 0, v3, vcc
	v_add_co_u32_e32 v16, vcc, s4, v2
	s_mov_b32 s4, 0x1c000
	s_nop 0
	v_addc_co_u32_e32 v17, vcc, 0, v3, vcc
	v_add_co_u32_e32 v18, vcc, s4, v2
	s_mov_b32 s4, 0x20000
	s_nop 0
	v_addc_co_u32_e32 v19, vcc, 0, v3, vcc
	global_load_dword v21, v[2:3], off nt
	global_load_dword v22, v[4:5], off nt
	global_load_dword v23, v[6:7], off nt
	global_load_dword v24, v[8:9], off nt
	global_load_dword v25, v[12:13], off nt
	global_load_dword v26, v[14:15], off nt
	global_load_dword v27, v[16:17], off nt
	global_load_dword v28, v[18:19], off nt
	v_add_co_u32_e32 v4, vcc, s4, v2
	s_mov_b32 s4, 0x24000
	s_nop 0
	v_addc_co_u32_e32 v5, vcc, 0, v3, vcc
	v_add_co_u32_e32 v6, vcc, s4, v2
	s_mov_b32 s4, 0x28000
	s_nop 0
	v_addc_co_u32_e32 v7, vcc, 0, v3, vcc
	v_add_co_u32_e32 v8, vcc, s4, v2
	s_mov_b32 s4, 0x2c000
	s_nop 0
	v_addc_co_u32_e32 v9, vcc, 0, v3, vcc
	v_add_co_u32_e32 v12, vcc, s4, v2
	s_mov_b32 s4, 0x30000
	s_nop 0
	v_addc_co_u32_e32 v13, vcc, 0, v3, vcc
	global_load_dword v14, v[4:5], off nt
	global_load_dword v15, v[6:7], off nt
	global_load_dword v16, v[8:9], off nt
	global_load_dword v17, v[12:13], off nt
	v_add_co_u32_e32 v4, vcc, s4, v2
	s_mov_b32 s4, 0x34000
	s_nop 0
	v_addc_co_u32_e32 v5, vcc, 0, v3, vcc
	v_add_co_u32_e32 v6, vcc, s4, v2
	s_mov_b32 s4, 0x38000
	s_nop 0
	v_addc_co_u32_e32 v7, vcc, 0, v3, vcc
	v_add_co_u32_e32 v8, vcc, s4, v2
	s_mov_b32 s4, 0x3c000
	s_nop 0
	v_addc_co_u32_e32 v9, vcc, 0, v3, vcc
	v_add_co_u32_e32 v2, vcc, s4, v2
	global_load_dword v12, v[4:5], off nt
	global_load_dword v13, v[6:7], off nt
	global_load_dword v18, v[8:9], off nt
	v_addc_co_u32_e32 v3, vcc, 0, v3, vcc
	global_load_dword v6, v[2:3], off nt
	s_load_dwordx2 s[16:17], s[0:1], 0x30
	s_movk_i32 s4, 0x840
	v_mad_u32_u24 v7, v1, s4, v10
	v_cmp_gt_u32_e32 vcc, 32, v0
	s_waitcnt vmcnt(15)
	v_cvt_f64_f32_e32 v[2:3], v21
	s_waitcnt vmcnt(14)
	v_cvt_f64_f32_e32 v[4:5], v22
	v_mul_f64 v[4:5], v[4:5], v[4:5]
	v_fmac_f64_e32 v[4:5], v[2:3], v[2:3]
	s_waitcnt vmcnt(13)
	v_cvt_f64_f32_e32 v[2:3], v23
	v_fmac_f64_e32 v[4:5], v[2:3], v[2:3]
	s_waitcnt vmcnt(12)
	v_cvt_f64_f32_e32 v[2:3], v24
	v_fmac_f64_e32 v[4:5], v[2:3], v[2:3]
	s_waitcnt vmcnt(11)
	v_cvt_f64_f32_e32 v[2:3], v25
	v_fmac_f64_e32 v[4:5], v[2:3], v[2:3]
	s_waitcnt vmcnt(10)
	v_cvt_f64_f32_e32 v[2:3], v26
	v_fmac_f64_e32 v[4:5], v[2:3], v[2:3]
	s_waitcnt vmcnt(9)
	v_cvt_f64_f32_e32 v[2:3], v27
	v_fmac_f64_e32 v[4:5], v[2:3], v[2:3]
	s_waitcnt vmcnt(8)
	v_cvt_f64_f32_e32 v[2:3], v28
	v_fmac_f64_e32 v[4:5], v[2:3], v[2:3]
	ds_write2_b32 v7, v21, v22 offset1:33
	ds_write2_b32 v7, v23, v24 offset0:66 offset1:99
	ds_write2_b32 v7, v25, v26 offset0:132 offset1:165
	ds_write2_b32 v7, v27, v28 offset0:198 offset1:231
	v_add_u32_e32 v7, 0x400, v7
	s_waitcnt vmcnt(7)
	v_cvt_f64_f32_e32 v[2:3], v14
	v_fmac_f64_e32 v[4:5], v[2:3], v[2:3]
	s_waitcnt vmcnt(6)
	v_cvt_f64_f32_e32 v[2:3], v15
	v_fmac_f64_e32 v[4:5], v[2:3], v[2:3]
	s_waitcnt vmcnt(5)
	v_cvt_f64_f32_e32 v[2:3], v16
	v_fmac_f64_e32 v[4:5], v[2:3], v[2:3]
	s_waitcnt vmcnt(4)
	v_cvt_f64_f32_e32 v[2:3], v17
	v_fmac_f64_e32 v[4:5], v[2:3], v[2:3]
	ds_write2_b32 v7, v14, v15 offset0:8 offset1:41
	ds_write2_b32 v7, v16, v17 offset0:74 offset1:107
	s_waitcnt vmcnt(3)
	v_cvt_f64_f32_e32 v[2:3], v12
	v_fmac_f64_e32 v[4:5], v[2:3], v[2:3]
	s_waitcnt vmcnt(2)
	v_cvt_f64_f32_e32 v[2:3], v13
	v_fmac_f64_e32 v[4:5], v[2:3], v[2:3]
	s_waitcnt vmcnt(1)
	v_cvt_f64_f32_e32 v[2:3], v18
	v_fmac_f64_e32 v[4:5], v[2:3], v[2:3]
	s_waitcnt vmcnt(0)
	v_cvt_f64_f32_e32 v[2:3], v6
	v_fmac_f64_e32 v[4:5], v[2:3], v[2:3]
	v_lshlrev_b32_e32 v2, 3, v20
	v_lshl_or_b32 v2, v1, 8, v2
	ds_write2_b32 v7, v12, v13 offset0:140 offset1:173
	ds_write2_b32 v7, v18, v6 offset0:206 offset1:239
	ds_write_b64 v2, v[4:5] offset:16896
	s_waitcnt lgkmcnt(0)
	s_barrier
	s_and_saveexec_b64 s[4:5], vcc
	s_cbranch_execz .LBB0_2
	s_load_dwordx4 s[24:27], s[0:1], 0x20
	v_lshlrev_b32_e32 v10, 3, v0
	v_add_u32_e32 v12, 0x4000, v10
	v_add_u32_e32 v16, 0x4800, v10
	ds_read2_b64 v[2:5], v12 offset0:64 offset1:96
	ds_read2_b64 v[6:9], v12 offset0:128 offset1:160
	ds_read2_b64 v[12:15], v12 offset0:192 offset1:224
	ds_read2_b64 v[16:19], v16 offset1:32
	s_and_b64 s[6:7], s[14:15], exec
	s_waitcnt lgkmcnt(0)
	s_cselect_b32 s6, s25, s27
	s_cselect_b32 s7, s24, s26
	s_lshl_b32 s21, s20, 15
	s_add_u32 s7, s7, s21
	v_add_f64 v[2:3], v[2:3], v[4:5]
	v_add_f64 v[4:5], v[6:7], v[8:9]
	s_addc_u32 s21, s6, 0
	s_lshl_b32 s6, s18, 3
	v_add_f64 v[2:3], v[2:3], v[4:5]
	v_add_f64 v[4:5], v[12:13], v[14:15]
	v_add_f64 v[6:7], v[16:17], v[18:19]
	s_add_u32 s6, s7, s6
	v_add_f64 v[4:5], v[4:5], v[6:7]
	s_addc_u32 s7, s21, 0
	v_add_f64 v[2:3], v[2:3], v[4:5]
	global_store_dwordx2 v10, v[2:3], s[6:7]

	.amdhsa_kernel _Z6k_prepPKfS0_PfS1_PdS2_PtS3_S3_
		.amdhsa_group_segment_fixed_size 18944
		.amdhsa_private_segment_fixed_size 0
		.amdhsa_kernarg_size 72
		.amdhsa_user_sgpr_count 2
		.amdhsa_user_sgpr_dispatch_ptr 0
		.amdhsa_user_sgpr_queue_ptr 0
		.amdhsa_user_sgpr_kernarg_segment_ptr 1
		.amdhsa_user_sgpr_dispatch_id 0
		.amdhsa_user_sgpr_kernarg_preload_length 0
		.amdhsa_user_sgpr_kernarg_preload_offset 0
		.amdhsa_user_sgpr_private_segment_size 0
		.amdhsa_uses_dynamic_stack 0
		.amdhsa_enable_private_segment 0
		.amdhsa_system_sgpr_workgroup_id_x 1
		.amdhsa_system_sgpr_workgroup_id_y 0
		.amdhsa_system_sgpr_workgroup_id_z 0
		.amdhsa_system_sgpr_workgroup_info 0
		.amdhsa_system_vgpr_workitem_id 0
		.amdhsa_next_free_vgpr 32
		.amdhsa_next_free_sgpr 30
		.amdhsa_accum_offset 32
		.amdhsa_reserve_vcc 1
		.amdhsa_float_round_mode_32 0
		.amdhsa_float_round_mode_16_64 0
		.amdhsa_float_denorm_mode_32 3
		.amdhsa_float_denorm_mode_16_64 3
		.amdhsa_dx10_clamp 1
		.amdhsa_ieee_mode 1
		.amdhsa_fp16_overflow 0
		.amdhsa_tg_split 0
		.amdhsa_exception_fp_ieee_invalid_op 0
		.amdhsa_exception_fp_denorm_src 0
		.amdhsa_exception_fp_ieee_div_zero 0
		.amdhsa_exception_fp_ieee_overflow 0
		.amdhsa_exception_fp_ieee_underflow 0
		.amdhsa_exception_fp_ieee_inexact 0
		.amdhsa_exception_int_div_zero 0
	.end_amdhsa_kernel

amdhsa.kernels:
  - .agpr_count:     0
    .args:
      - .actual_access:  read_only
        .address_space:  global
        .offset:         0
        .size:           8
        .value_kind:     global_buffer
      - .actual_access:  read_only
        .address_space:  global
        .offset:         8
        .size:           8
        .value_kind:     global_buffer
      - .actual_access:  write_only
        .address_space:  global
        .offset:         16
        .size:           8
        .value_kind:     global_buffer
      - .actual_access:  write_only
        .address_space:  global
        .offset:         24
        .size:           8
        .value_kind:     global_buffer
      - .actual_access:  write_only
        .address_space:  global
        .offset:         32
        .size:           8
        .value_kind:     global_buffer
      - .actual_access:  write_only
        .address_space:  global
        .offset:         40
        .size:           8
        .value_kind:     global_buffer
      - .actual_access:  write_only
        .address_space:  global
        .offset:         48
        .size:           8
        .value_kind:     global_buffer
      - .actual_access:  write_only
        .address_space:  global
        .offset:         56
        .size:           8
        .value_kind:     global_buffer
      - .actual_access:  write_only
        .address_space:  global
        .offset:         64
        .size:           8
        .value_kind:     global_buffer
    .group_segment_fixed_size: 18944
    .kernarg_segment_align: 8
    .kernarg_segment_size: 72
    .language:       OpenCL C
    .language_version:
      - 2
      - 0
    .max_flat_workgroup_size: 256
    .name:           _Z6k_prepPKfS0_PfS1_PdS2_PtS3_S3_
    .private_segment_fixed_size: 0
    .sgpr_count:     36
    .sgpr_spill_count: 0
    .symbol:         _Z6k_prepPKfS0_PfS1_PdS2_PtS3_S3_.kd
    .uniform_work_group_size: 1
    .uses_dynamic_stack: false
    .vgpr_count:     32
    .vgpr_spill_count: 0
    .wavefront_size: 64
  - .agpr_count:     16
    .args:
      - .actual_access:  read_only
        .address_space:  global
        .offset:         0
        .size:           8
        .value_kind:     global_buffer
      - .actual_access:  read_only
        .address_space:  global
        .offset:         8
        .size:           8
        .value_kind:     global_buffer
      - .actual_access:  read_only
        .address_space:  global
        .offset:         16
        .size:           8
        .value_kind:     global_buffer
      - .actual_access:  read_only
        .address_space:  global
        .offset:         24
        .size:           8
        .value_kind:     global_buffer
      - .actual_access:  write_only
        .address_space:  global
        .offset:         32
        .size:           8
        .value_kind:     global_buffer
    .group_segment_fixed_size: 256
    .kernarg_segment_align: 8
    .kernarg_segment_size: 40
    .language:       OpenCL C
    .language_version:
      - 2
      - 0
    .max_flat_workgroup_size: 256
    .name:           _Z9k_coarse2PKtS0_PKdS2_Pf
    .private_segment_fixed_size: 0
    .sgpr_count:     37
    .sgpr_spill_count: 0
    .symbol:         _Z9k_coarse2PKtS0_PKdS2_Pf.kd
    .uniform_work_group_size: 1
    .uses_dynamic_stack: false
    .vgpr_count:     156
    .vgpr_spill_count: 0
    .wavefront_size: 64
  - .agpr_count:     0
    .args:
      - .actual_access:  read_only
        .address_space:  global
        .offset:         0
        .size:           8
        .value_kind:     global_buffer
      - .actual_access:  read_only
        .address_space:  global
        .offset:         8
        .size:           8
        .value_kind:     global_buffer
      - .actual_access:  read_only
        .address_space:  global
        .offset:         16
        .size:           8
        .value_kind:     global_buffer
      - .actual_access:  read_only
        .address_space:  global
        .offset:         24
        .size:           8
        .value_kind:     global_buffer
      - .actual_access:  read_only
        .address_space:  global
        .offset:         32
        .size:           8
        .value_kind:     global_buffer
      - .actual_access:  read_only
        .address_space:  global
        .offset:         40
        .size:           8
        .value_kind:     global_buffer
      - .actual_access:  read_only
        .address_space:  global
        .offset:         48
        .size:           8
        .value_kind:     global_buffer
      - .actual_access:  write_only
        .address_space:  global
        .offset:         56
        .size:           8
        .value_kind:     global_buffer
      - .actual_access:  write_only
        .address_space:  global
        .offset:         64
        .size:           8
        .value_kind:     global_buffer
      - .actual_access:  write_only
        .address_space:  global
        .offset:         72
        .size:           8
        .value_kind:     global_buffer
      - .actual_access:  read_only
        .address_space:  global
        .offset:         80
        .size:           8
        .value_kind:     global_buffer
      - .actual_access:  read_only
        .address_space:  global
        .offset:         88
        .size:           8
        .value_kind:     global_buffer
      - .actual_access:  write_only
        .address_space:  global
        .offset:         96
        .size:           8
        .value_kind:     global_buffer
      - .actual_access:  write_only
        .address_space:  global
        .offset:         104
        .size:           8
        .value_kind:     global_buffer
    .group_segment_fixed_size: 30768
    .kernarg_segment_align: 8
    .kernarg_segment_size: 112
    .language:       OpenCL C
    .language_version:
      - 2
      - 0
    .max_flat_workgroup_size: 512
    .name:           _Z7k_fine3PKfS0_PKtS2_PKdS4_S0_PiPfS5_S0_S0_PtS7_
    .private_segment_fixed_size: 0
    .sgpr_count:     106
    .sgpr_spill_count: 4
    .symbol:         _Z7k_fine3PKfS0_PKtS2_PKdS4_S0_PiPfS5_S0_S0_PtS7_.kd
    .uniform_work_group_size: 1
    .uses_dynamic_stack: false
    .vgpr_count:     256
    .vgpr_spill_count: 0
    .wavefront_size: 64
  - .agpr_count:     0
    .args:
      - .actual_access:  read_only
        .address_space:  global
        .offset:         0
        .size:           8
        .value_kind:     global_buffer
      - .actual_access:  read_only
        .address_space:  global
        .offset:         8
        .size:           8
        .value_kind:     global_buffer
      - .actual_access:  read_only
        .address_space:  global
        .offset:         16
        .size:           8
        .value_kind:     global_buffer
      - .actual_access:  read_only
        .address_space:  global
        .offset:         24
        .size:           8
        .value_kind:     global_buffer
      - .actual_access:  read_only
        .address_space:  global
        .offset:         32
        .size:           8
        .value_kind:     global_buffer
      - .actual_access:  read_only
        .address_space:  global
        .offset:         40
        .size:           8
        .value_kind:     global_buffer
      - .actual_access:  write_only
        .address_space:  global
        .offset:         48
        .size:           8
        .value_kind:     global_buffer
      - .actual_access:  write_only
        .address_space:  global
        .offset:         56
        .size:           8
        .value_kind:     global_buffer
      - .actual_access:  write_only
        .address_space:  global
        .offset:         64
        .size:           8
        .value_kind:     global_buffer
    .group_segment_fixed_size: 18512
    .kernarg_segment_align: 8
    .kernarg_segment_size: 72
    .language:       OpenCL C
    .language_version:
      - 2
      - 0
    .max_flat_workgroup_size: 256
    .name:           _Z10k_transferPKtS0_PKfPKiS2_S4_PfS5_S5_
    .private_segment_fixed_size: 0
    .sgpr_count:     34
    .sgpr_spill_count: 0
    .symbol:         _Z10k_transferPKtS0_PKfPKiS2_S4_PfS5_S5_.kd
    .uniform_work_group_size: 1
    .uses_dynamic_stack: false
    .vgpr_count:     49
    .vgpr_spill_count: 0
    .wavefront_size: 64
